# router phase: first batch's X1 row loads issued in the preheader after the second router-weight load group (its waits relaxed by 8); loop-top copy skipped for that batch
# speedup vs baseline: 1.0011x; 1.0011x over previous
.LBB0_476:
	s_cmpk_gt_i32 s72, 0xff
	s_cbranch_scc1 .LBB0_491
	s_load_dwordx4 s[40:43], s[0:1], 0x58
	s_load_dwordx2 s[38:39], s[0:1], 0x50
	s_load_dwordx2 s[26:27], s[0:1], 0x98
	s_ashr_i32 s83, s82, 31
	s_waitcnt vmcnt(0)
	v_ashrrev_i32_e32 v87, 5, v194
	v_readlane_b32 s6, v253, 16
	s_lshl_b64 s[4:5], s[82:83], 17
	s_waitcnt lgkmcnt(0)
	s_add_u32 s4, s40, s4
	v_lshl_add_u32 v4, v87, 3, s6
	v_and_b32_e32 v82, 31, v194
	v_add_u32_e32 v12, 0x73, v4
	s_addc_u32 s5, s41, s5
	v_lshlrev_b32_e32 v0, 2, v82
	v_ashrrev_i32_e32 v13, 31, v12
	v_lshl_add_u64 v[2:3], s[4:5], 0, v[0:1]
	v_lshlrev_b64 v[12:13], 7, v[12:13]
	v_lshl_add_u64 v[16:17], v[2:3], 0, v[12:13]
	v_add_u32_e32 v12, 0x74, v4
	v_ashrrev_i32_e32 v13, 31, v12
	v_lshlrev_b64 v[12:13], 7, v[12:13]
	v_lshl_add_u64 v[18:19], v[2:3], 0, v[12:13]
	v_add_u32_e32 v12, 0x75, v4
	v_ashrrev_i32_e32 v13, 31, v12
	v_lshlrev_b64 v[12:13], 7, v[12:13]
	v_lshl_add_u64 v[20:21], v[2:3], 0, v[12:13]
	v_add_u32_e32 v12, 0x76, v4
	s_lshl_b32 s14, s82, 5
	v_ashrrev_i32_e32 v13, 31, v12
	s_ashr_i32 s15, s14, 31
	v_add_u32_e32 v6, 0x70, v4
	v_add_u32_e32 v8, 0x71, v4
	v_add_u32_e32 v10, 0x72, v4
	v_lshlrev_b64 v[12:13], 7, v[12:13]
	s_lshl_b64 s[14:15], s[14:15], 2
	v_ashrrev_i32_e32 v7, 31, v6
	v_ashrrev_i32_e32 v9, 31, v8
	v_ashrrev_i32_e32 v11, 31, v10
	v_lshl_add_u64 v[22:23], v[2:3], 0, v[12:13]
	v_add_u32_e32 v12, 0x77, v4
	s_add_u32 s14, s42, s14
	v_lshlrev_b64 v[6:7], 7, v[6:7]
	v_lshlrev_b64 v[8:9], 7, v[8:9]
	v_lshlrev_b64 v[10:11], 7, v[10:11]
	v_ashrrev_i32_e32 v13, 31, v12
	s_addc_u32 s15, s43, s15
	v_lshl_add_u64 v[6:7], v[2:3], 0, v[6:7]
	v_lshl_add_u64 v[8:9], v[2:3], 0, v[8:9]
	v_lshl_add_u64 v[10:11], v[2:3], 0, v[10:11]
	v_lshlrev_b64 v[12:13], 7, v[12:13]
	global_load_dword v83, v0, s[14:15]
	v_lshl_add_u64 v[24:25], v[2:3], 0, v[12:13]
	global_load_dword v14, v[6:7], off
	global_load_dword v15, v[8:9], off
	global_load_dword v12, v[10:11], off
	global_load_dword v13, v[16:17], off
	s_nop 0
	global_load_dword v10, v[18:19], off
	global_load_dword v11, v[20:21], off
	global_load_dword v8, v[22:23], off
	global_load_dword v9, v[24:25], off
	v_add_u32_e32 v6, 0x60, v4
	v_add_u32_e32 v16, 0x61, v4
	v_ashrrev_i32_e32 v7, 31, v6
	v_ashrrev_i32_e32 v17, 31, v16
	v_add_u32_e32 v18, 0x62, v4
	v_add_u32_e32 v20, 0x63, v4
	v_add_u32_e32 v22, 0x64, v4
	v_add_u32_e32 v24, 0x65, v4
	v_add_u32_e32 v26, 0x66, v4
	v_add_u32_e32 v28, 0x67, v4
	v_lshlrev_b64 v[6:7], 7, v[6:7]
	v_lshlrev_b64 v[16:17], 7, v[16:17]
	v_ashrrev_i32_e32 v19, 31, v18
	v_ashrrev_i32_e32 v21, 31, v20
	v_ashrrev_i32_e32 v23, 31, v22
	v_ashrrev_i32_e32 v25, 31, v24
	v_ashrrev_i32_e32 v27, 31, v26
	v_ashrrev_i32_e32 v29, 31, v28
	v_lshl_add_u64 v[6:7], v[2:3], 0, v[6:7]
	v_lshl_add_u64 v[16:17], v[2:3], 0, v[16:17]
	v_lshlrev_b64 v[18:19], 7, v[18:19]
	v_lshlrev_b64 v[20:21], 7, v[20:21]
	v_lshlrev_b64 v[22:23], 7, v[22:23]
	v_lshlrev_b64 v[24:25], 7, v[24:25]
	v_lshlrev_b64 v[26:27], 7, v[26:27]
	v_lshlrev_b64 v[28:29], 7, v[28:29]
	v_lshl_add_u64 v[18:19], v[2:3], 0, v[18:19]
	v_lshl_add_u64 v[20:21], v[2:3], 0, v[20:21]
	v_lshl_add_u64 v[22:23], v[2:3], 0, v[22:23]
	v_lshl_add_u64 v[24:25], v[2:3], 0, v[24:25]
	v_lshl_add_u64 v[26:27], v[2:3], 0, v[26:27]
	v_lshl_add_u64 v[28:29], v[2:3], 0, v[28:29]
	global_load_dword v30, v[6:7], off
	global_load_dword v31, v[16:17], off
	global_load_dword v34, v[18:19], off
	global_load_dword v35, v[20:21], off
	global_load_dword v32, v[22:23], off
	global_load_dword v33, v[24:25], off
	s_nop 0
	global_load_dword v16, v[26:27], off
	global_load_dword v17, v[28:29], off
	v_add_u32_e32 v6, 0x50, v4
	v_ashrrev_i32_e32 v7, 31, v6
	v_add_u32_e32 v18, 0x51, v4
	v_add_u32_e32 v20, 0x52, v4
	v_add_u32_e32 v22, 0x53, v4
	v_add_u32_e32 v24, 0x54, v4
	v_add_u32_e32 v26, 0x55, v4
	v_add_u32_e32 v28, 0x56, v4
	v_add_u32_e32 v36, 0x57, v4
	v_lshlrev_b64 v[6:7], 7, v[6:7]
	v_ashrrev_i32_e32 v19, 31, v18
	v_ashrrev_i32_e32 v21, 31, v20
	v_ashrrev_i32_e32 v23, 31, v22
	v_ashrrev_i32_e32 v25, 31, v24
	v_ashrrev_i32_e32 v27, 31, v26
	v_ashrrev_i32_e32 v29, 31, v28
	v_ashrrev_i32_e32 v37, 31, v36
	v_lshl_add_u64 v[6:7], v[2:3], 0, v[6:7]
	v_lshlrev_b64 v[18:19], 7, v[18:19]
	v_lshlrev_b64 v[20:21], 7, v[20:21]
	v_lshlrev_b64 v[22:23], 7, v[22:23]
	v_lshlrev_b64 v[24:25], 7, v[24:25]
	v_lshlrev_b64 v[26:27], 7, v[26:27]
	v_lshlrev_b64 v[28:29], 7, v[28:29]
	v_lshlrev_b64 v[36:37], 7, v[36:37]
	v_lshl_add_u64 v[18:19], v[2:3], 0, v[18:19]
	v_lshl_add_u64 v[20:21], v[2:3], 0, v[20:21]
	v_lshl_add_u64 v[22:23], v[2:3], 0, v[22:23]
	v_lshl_add_u64 v[24:25], v[2:3], 0, v[24:25]
	v_lshl_add_u64 v[26:27], v[2:3], 0, v[26:27]
	v_lshl_add_u64 v[28:29], v[2:3], 0, v[28:29]
	v_lshl_add_u64 v[36:37], v[2:3], 0, v[36:37]
	global_load_dword v38, v[6:7], off
	global_load_dword v39, v[18:19], off
	global_load_dword v40, v[20:21], off
	global_load_dword v41, v[22:23], off
	global_load_dword v42, v[24:25], off
	global_load_dword v43, v[26:27], off
	global_load_dword v44, v[28:29], off
	global_load_dword v45, v[36:37], off
	v_add_u32_e32 v6, 64, v4
	v_ashrrev_i32_e32 v7, 31, v6
	v_add_u32_e32 v18, 0x41, v4
	v_lshlrev_b64 v[6:7], 7, v[6:7]
	v_ashrrev_i32_e32 v19, 31, v18
	v_lshl_add_u64 v[6:7], v[2:3], 0, v[6:7]
	v_lshlrev_b64 v[18:19], 7, v[18:19]
	v_lshl_add_u64 v[18:19], v[2:3], 0, v[18:19]
	global_load_dword v46, v[6:7], off
	global_load_dword v47, v[18:19], off
	v_add_u32_e32 v6, 0x42, v4
	v_ashrrev_i32_e32 v7, 31, v6
	v_add_u32_e32 v18, 0x43, v4
	v_add_u32_e32 v20, 0x44, v4
	v_add_u32_e32 v22, 0x45, v4
	v_lshlrev_b64 v[6:7], 7, v[6:7]
	v_ashrrev_i32_e32 v19, 31, v18
	v_ashrrev_i32_e32 v21, 31, v20
	v_ashrrev_i32_e32 v23, 31, v22
	v_lshl_add_u64 v[6:7], v[2:3], 0, v[6:7]
	v_lshlrev_b64 v[18:19], 7, v[18:19]
	v_lshlrev_b64 v[20:21], 7, v[20:21]
	v_lshlrev_b64 v[22:23], 7, v[22:23]
	v_lshl_add_u64 v[18:19], v[2:3], 0, v[18:19]
	v_lshl_add_u64 v[20:21], v[2:3], 0, v[20:21]
	v_lshl_add_u64 v[22:23], v[2:3], 0, v[22:23]
	global_load_dword v48, v[6:7], off
	global_load_dword v49, v[18:19], off
	global_load_dword v50, v[20:21], off
	global_load_dword v51, v[22:23], off
	v_add_u32_e32 v6, 0x46, v4
	v_add_u32_e32 v18, 0x47, v4
	v_ashrrev_i32_e32 v7, 31, v6
	v_ashrrev_i32_e32 v19, 31, v18
	v_lshlrev_b64 v[6:7], 7, v[6:7]
	v_lshlrev_b64 v[18:19], 7, v[18:19]
	v_lshl_add_u64 v[6:7], v[2:3], 0, v[6:7]
	v_lshl_add_u64 v[18:19], v[2:3], 0, v[18:19]
	global_load_dword v6, v[6:7], off
	s_nop 0
	global_load_dword v7, v[18:19], off
	s_waitcnt vmcnt(30)
	v_cvt_pk_bf16_f32 v18, v14, v15
	v_lshlrev_b32_e32 v20, 16, v18
	v_and_b32_e32 v21, 0xffff0000, v18
	v_pk_add_f32 v[14:15], v[14:15], v[20:21] neg_lo:[0,1] neg_hi:[0,1]
	s_waitcnt vmcnt(28)
	v_cvt_pk_bf16_f32 v19, v12, v13
	v_cvt_pk_bf16_f32 v22, v14, v15
	v_lshlrev_b32_e32 v14, 16, v19
	v_and_b32_e32 v15, 0xffff0000, v19
	v_pk_add_f32 v[12:13], v[12:13], v[14:15] neg_lo:[0,1] neg_hi:[0,1]
	s_waitcnt vmcnt(26)
	v_cvt_pk_bf16_f32 v20, v10, v11
	v_cvt_pk_bf16_f32 v23, v12, v13
	v_lshlrev_b32_e32 v12, 16, v20
	v_and_b32_e32 v13, 0xffff0000, v20
	v_pk_add_f32 v[10:11], v[10:11], v[12:13] neg_lo:[0,1] neg_hi:[0,1]
	s_waitcnt vmcnt(24)
	v_cvt_pk_bf16_f32 v21, v8, v9
	v_cvt_pk_bf16_f32 v24, v10, v11
	v_lshlrev_b32_e32 v10, 16, v21
	v_and_b32_e32 v11, 0xffff0000, v21
	v_pk_add_f32 v[8:9], v[8:9], v[10:11] neg_lo:[0,1] neg_hi:[0,1]
	s_waitcnt vmcnt(22)
	v_cvt_pk_bf16_f32 v26, v30, v31
	v_cvt_pk_bf16_f32 v25, v8, v9
	v_lshlrev_b32_e32 v8, 16, v26
	v_and_b32_e32 v9, 0xffff0000, v26
	v_pk_add_f32 v[8:9], v[30:31], v[8:9] neg_lo:[0,1] neg_hi:[0,1]
	s_waitcnt vmcnt(20)
	v_cvt_pk_bf16_f32 v27, v34, v35
	v_cvt_pk_bf16_f32 v30, v8, v9
	v_lshlrev_b32_e32 v8, 16, v27
	v_and_b32_e32 v9, 0xffff0000, v27
	v_pk_add_f32 v[8:9], v[34:35], v[8:9] neg_lo:[0,1] neg_hi:[0,1]
	s_waitcnt vmcnt(18)
	v_cvt_pk_bf16_f32 v28, v32, v33
	v_cvt_pk_bf16_f32 v31, v8, v9
	v_lshlrev_b32_e32 v8, 16, v28
	v_and_b32_e32 v9, 0xffff0000, v28
	v_pk_add_f32 v[8:9], v[32:33], v[8:9] neg_lo:[0,1] neg_hi:[0,1]
	s_waitcnt vmcnt(16)
	v_cvt_pk_bf16_f32 v29, v16, v17
	v_cvt_pk_bf16_f32 v32, v8, v9
	v_lshlrev_b32_e32 v8, 16, v29
	v_and_b32_e32 v9, 0xffff0000, v29
	v_pk_add_f32 v[8:9], v[16:17], v[8:9] neg_lo:[0,1] neg_hi:[0,1]
	s_waitcnt vmcnt(14)
	v_cvt_pk_bf16_f32 v34, v38, v39
	v_cvt_pk_bf16_f32 v33, v8, v9
	v_lshlrev_b32_e32 v8, 16, v34
	v_and_b32_e32 v9, 0xffff0000, v34
	v_pk_add_f32 v[8:9], v[38:39], v[8:9] neg_lo:[0,1] neg_hi:[0,1]
	s_waitcnt vmcnt(12)
	v_cvt_pk_bf16_f32 v35, v40, v41
	v_cvt_pk_bf16_f32 v38, v8, v9
	v_lshlrev_b32_e32 v8, 16, v35
	v_and_b32_e32 v9, 0xffff0000, v35
	v_pk_add_f32 v[8:9], v[40:41], v[8:9] neg_lo:[0,1] neg_hi:[0,1]
	s_waitcnt vmcnt(10)
	v_cvt_pk_bf16_f32 v36, v42, v43
	v_cvt_pk_bf16_f32 v39, v8, v9
	v_lshlrev_b32_e32 v8, 16, v36
	v_and_b32_e32 v9, 0xffff0000, v36
	v_pk_add_f32 v[8:9], v[42:43], v[8:9] neg_lo:[0,1] neg_hi:[0,1]
	s_waitcnt vmcnt(8)
	v_cvt_pk_bf16_f32 v37, v44, v45
	v_cvt_pk_bf16_f32 v40, v8, v9
	v_lshlrev_b32_e32 v8, 16, v37
	v_and_b32_e32 v9, 0xffff0000, v37
	v_pk_add_f32 v[8:9], v[44:45], v[8:9] neg_lo:[0,1] neg_hi:[0,1]
	s_waitcnt vmcnt(6)
	v_cvt_pk_bf16_f32 v42, v46, v47
	v_add_u32_e32 v14, 51, v4
	v_cvt_pk_bf16_f32 v41, v8, v9
	v_lshlrev_b32_e32 v8, 16, v42
	v_and_b32_e32 v9, 0xffff0000, v42
	v_ashrrev_i32_e32 v15, 31, v14
	v_pk_add_f32 v[8:9], v[46:47], v[8:9] neg_lo:[0,1] neg_hi:[0,1]
	v_lshlrev_b64 v[14:15], 7, v[14:15]
	v_cvt_pk_bf16_f32 v46, v8, v9
	s_waitcnt vmcnt(4)
	v_cvt_pk_bf16_f32 v43, v48, v49
	v_lshlrev_b32_e32 v8, 16, v43
	v_and_b32_e32 v9, 0xffff0000, v43
	v_lshl_add_u64 v[16:17], v[2:3], 0, v[14:15]
	v_add_u32_e32 v14, 52, v4
	v_pk_add_f32 v[8:9], v[48:49], v[8:9] neg_lo:[0,1] neg_hi:[0,1]
	s_waitcnt vmcnt(2)
	v_cvt_pk_bf16_f32 v44, v50, v51
	v_ashrrev_i32_e32 v15, 31, v14
	v_cvt_pk_bf16_f32 v47, v8, v9
	v_lshlrev_b32_e32 v8, 16, v44
	v_and_b32_e32 v9, 0xffff0000, v44
	v_lshlrev_b64 v[14:15], 7, v[14:15]
	v_pk_add_f32 v[8:9], v[50:51], v[8:9] neg_lo:[0,1] neg_hi:[0,1]
	v_lshl_add_u64 v[50:51], v[2:3], 0, v[14:15]
	v_add_u32_e32 v14, 53, v4
	v_ashrrev_i32_e32 v15, 31, v14
	v_lshlrev_b64 v[14:15], 7, v[14:15]
	v_lshl_add_u64 v[52:53], v[2:3], 0, v[14:15]
	v_add_u32_e32 v14, 54, v4
	v_ashrrev_i32_e32 v15, 31, v14
	v_cvt_pk_bf16_f32 v48, v8, v9
	v_add_u32_e32 v8, 48, v4
	v_add_u32_e32 v10, 49, v4
	v_add_u32_e32 v12, 50, v4
	v_lshlrev_b64 v[14:15], 7, v[14:15]
	v_ashrrev_i32_e32 v9, 31, v8
	v_ashrrev_i32_e32 v11, 31, v10
	v_ashrrev_i32_e32 v13, 31, v12
	v_lshl_add_u64 v[54:55], v[2:3], 0, v[14:15]
	v_add_u32_e32 v14, 55, v4
	v_lshlrev_b64 v[8:9], 7, v[8:9]
	v_lshlrev_b64 v[10:11], 7, v[10:11]
	v_lshlrev_b64 v[12:13], 7, v[12:13]
	v_ashrrev_i32_e32 v15, 31, v14
	v_lshl_add_u64 v[8:9], v[2:3], 0, v[8:9]
	v_lshl_add_u64 v[10:11], v[2:3], 0, v[10:11]
	v_lshl_add_u64 v[12:13], v[2:3], 0, v[12:13]
	v_lshlrev_b64 v[14:15], 7, v[14:15]
	v_lshl_add_u64 v[56:57], v[2:3], 0, v[14:15]
	global_load_dword v14, v[8:9], off
	global_load_dword v15, v[10:11], off
	s_nop 0
	global_load_dword v12, v[12:13], off
	s_nop 0
	global_load_dword v13, v[16:17], off
	global_load_dword v10, v[50:51], off
	global_load_dword v11, v[52:53], off
	global_load_dword v8, v[54:55], off
	global_load_dword v9, v[56:57], off
	v_add_u32_e32 v16, 32, v4
	v_ashrrev_i32_e32 v17, 31, v16
	v_add_u32_e32 v50, 33, v4
	v_add_u32_e32 v52, 34, v4
	v_add_u32_e32 v54, 35, v4
	v_add_u32_e32 v56, 36, v4
	v_add_u32_e32 v58, 37, v4
	v_add_u32_e32 v60, 38, v4
	v_add_u32_e32 v62, 39, v4
	v_lshlrev_b64 v[16:17], 7, v[16:17]
	v_ashrrev_i32_e32 v51, 31, v50
	v_ashrrev_i32_e32 v53, 31, v52
	v_ashrrev_i32_e32 v55, 31, v54
	v_ashrrev_i32_e32 v57, 31, v56
	v_ashrrev_i32_e32 v59, 31, v58
	v_ashrrev_i32_e32 v61, 31, v60
	v_ashrrev_i32_e32 v63, 31, v62
	v_lshl_add_u64 v[16:17], v[2:3], 0, v[16:17]
	v_lshlrev_b64 v[50:51], 7, v[50:51]
	v_lshlrev_b64 v[52:53], 7, v[52:53]
	v_lshlrev_b64 v[54:55], 7, v[54:55]
	v_lshlrev_b64 v[56:57], 7, v[56:57]
	v_lshlrev_b64 v[58:59], 7, v[58:59]
	v_lshlrev_b64 v[60:61], 7, v[60:61]
	v_lshlrev_b64 v[62:63], 7, v[62:63]
	v_lshl_add_u64 v[50:51], v[2:3], 0, v[50:51]
	v_lshl_add_u64 v[52:53], v[2:3], 0, v[52:53]
	v_lshl_add_u64 v[54:55], v[2:3], 0, v[54:55]
	v_lshl_add_u64 v[56:57], v[2:3], 0, v[56:57]
	v_lshl_add_u64 v[58:59], v[2:3], 0, v[58:59]
	v_lshl_add_u64 v[60:61], v[2:3], 0, v[60:61]
	v_lshl_add_u64 v[62:63], v[2:3], 0, v[62:63]
	global_load_dword v64, v[16:17], off
	global_load_dword v65, v[50:51], off
	global_load_dword v66, v[52:53], off
	global_load_dword v67, v[54:55], off
	global_load_dword v68, v[56:57], off
	global_load_dword v69, v[58:59], off
	global_load_dword v16, v[60:61], off
	global_load_dword v17, v[62:63], off
	v_add_u32_e32 v50, 16, v4
	v_add_u32_e32 v52, 17, v4
	v_ashrrev_i32_e32 v51, 31, v50
	v_ashrrev_i32_e32 v53, 31, v52
	v_add_u32_e32 v54, 18, v4
	v_add_u32_e32 v56, 19, v4
	v_add_u32_e32 v58, 20, v4
	v_add_u32_e32 v60, 21, v4
	v_add_u32_e32 v62, 22, v4
	v_add_u32_e32 v70, 23, v4
	v_lshlrev_b64 v[50:51], 7, v[50:51]
	v_lshlrev_b64 v[52:53], 7, v[52:53]
	v_ashrrev_i32_e32 v55, 31, v54
	v_ashrrev_i32_e32 v57, 31, v56
	v_ashrrev_i32_e32 v59, 31, v58
	v_ashrrev_i32_e32 v61, 31, v60
	v_ashrrev_i32_e32 v63, 31, v62
	v_ashrrev_i32_e32 v71, 31, v70
	v_lshl_add_u64 v[50:51], v[2:3], 0, v[50:51]
	v_lshl_add_u64 v[52:53], v[2:3], 0, v[52:53]
	v_lshlrev_b64 v[54:55], 7, v[54:55]
	v_lshlrev_b64 v[56:57], 7, v[56:57]
	v_lshlrev_b64 v[58:59], 7, v[58:59]
	v_lshlrev_b64 v[60:61], 7, v[60:61]
	v_lshlrev_b64 v[62:63], 7, v[62:63]
	v_lshlrev_b64 v[70:71], 7, v[70:71]
	v_lshl_add_u64 v[54:55], v[2:3], 0, v[54:55]
	v_lshl_add_u64 v[56:57], v[2:3], 0, v[56:57]
	v_lshl_add_u64 v[58:59], v[2:3], 0, v[58:59]
	v_lshl_add_u64 v[60:61], v[2:3], 0, v[60:61]
	v_lshl_add_u64 v[62:63], v[2:3], 0, v[62:63]
	v_lshl_add_u64 v[70:71], v[2:3], 0, v[70:71]
	global_load_dword v72, v[50:51], off
	global_load_dword v73, v[52:53], off
	global_load_dword v74, v[54:55], off
	global_load_dword v75, v[56:57], off
	global_load_dword v76, v[58:59], off
	global_load_dword v77, v[60:61], off
	global_load_dword v78, v[62:63], off
	global_load_dword v79, v[70:71], off
	v_ashrrev_i32_e32 v5, 31, v4
	v_or_b32_e32 v52, 1, v4
	v_lshlrev_b64 v[50:51], 7, v[4:5]
	v_ashrrev_i32_e32 v53, 31, v52
	v_lshl_add_u64 v[50:51], v[2:3], 0, v[50:51]
	v_lshlrev_b64 v[52:53], 7, v[52:53]
	v_lshl_add_u64 v[52:53], v[2:3], 0, v[52:53]
	global_load_dword v80, v[50:51], off
	global_load_dword v81, v[52:53], off
	v_or_b32_e32 v50, 2, v4
	v_ashrrev_i32_e32 v51, 31, v50
	v_or_b32_e32 v52, 3, v4
	v_or_b32_e32 v54, 4, v4
	v_or_b32_e32 v56, 5, v4
	v_lshlrev_b64 v[50:51], 7, v[50:51]
	v_ashrrev_i32_e32 v53, 31, v52
	v_ashrrev_i32_e32 v55, 31, v54
	v_ashrrev_i32_e32 v57, 31, v56
	v_lshl_add_u64 v[50:51], v[2:3], 0, v[50:51]
	v_lshlrev_b64 v[52:53], 7, v[52:53]
	v_lshlrev_b64 v[54:55], 7, v[54:55]
	v_lshlrev_b64 v[56:57], 7, v[56:57]
	v_lshl_add_u64 v[52:53], v[2:3], 0, v[52:53]
	v_lshl_add_u64 v[54:55], v[2:3], 0, v[54:55]
	v_lshl_add_u64 v[56:57], v[2:3], 0, v[56:57]
	global_load_dword v84, v[50:51], off
	global_load_dword v85, v[52:53], off
	global_load_dword v88, v[54:55], off
	global_load_dword v89, v[56:57], off
	v_or_b32_e32 v50, 6, v4
	v_ashrrev_i32_e32 v51, 31, v50
	v_or_b32_e32 v4, 7, v4
	v_lshlrev_b64 v[50:51], 7, v[50:51]
	v_ashrrev_i32_e32 v5, 31, v4
	v_lshl_add_u64 v[50:51], v[2:3], 0, v[50:51]
	v_lshlrev_b64 v[4:5], 7, v[4:5]
	v_lshl_add_u64 v[2:3], v[2:3], 0, v[4:5]
	global_load_dword v4, v[50:51], off
	global_load_dword v5, v[2:3], off
	v_lshlrev_b32_e32 v124, 3, v194
	v_mov_b32_e32 v125, 0
	v_lshl_add_u64 v[124:125], s[26:27], 0, v[124:125]
	s_mov_b64 s[100:101], 0x26000000
	v_lshl_add_u64 v[124:125], v[124:125], 0, s[100:101]
	s_lshl_b32 s100, s72, 6
	s_add_i32 s100, s100, s61
	s_lshl_b32 s100, s100, 11
	s_mov_b32 s101, 0
	v_lshl_add_u64 v[124:125], v[124:125], 0, s[100:101]
	global_load_dwordx2 v[102:103], v[124:125], off nt
	global_load_dwordx2 v[104:105], v[124:125], off offset:512 nt
	global_load_dwordx2 v[106:107], v[124:125], off offset:1024 nt
	global_load_dwordx2 v[108:109], v[124:125], off offset:1536 nt
	global_load_dwordx2 v[112:113], v[124:125], off offset:2048 nt
	global_load_dwordx2 v[118:119], v[124:125], off offset:2560 nt
	global_load_dwordx2 v[120:121], v[124:125], off offset:3072 nt
	global_load_dwordx2 v[122:123], v[124:125], off offset:3584 nt
	s_mov_b32 s100, 1
	s_waitcnt vmcnt(40)
	v_cvt_pk_bf16_f32 v45, v6, v7
	v_lshlrev_b32_e32 v2, 16, v45
	v_and_b32_e32 v3, 0xffff0000, v45
	v_pk_add_f32 v[2:3], v[6:7], v[2:3] neg_lo:[0,1] neg_hi:[0,1]
	s_waitcnt vmcnt(38)
	v_cvt_pk_bf16_f32 v50, v14, v15
	v_cvt_pk_bf16_f32 v49, v2, v3
	v_lshlrev_b32_e32 v2, 16, v50
	v_and_b32_e32 v3, 0xffff0000, v50
	v_pk_add_f32 v[2:3], v[14:15], v[2:3] neg_lo:[0,1] neg_hi:[0,1]
	s_waitcnt vmcnt(36)
	v_cvt_pk_bf16_f32 v51, v12, v13
	v_cvt_pk_bf16_f32 v54, v2, v3
	v_lshlrev_b32_e32 v2, 16, v51
	v_and_b32_e32 v3, 0xffff0000, v51
	v_pk_add_f32 v[2:3], v[12:13], v[2:3] neg_lo:[0,1] neg_hi:[0,1]
	s_waitcnt vmcnt(34)
	v_cvt_pk_bf16_f32 v52, v10, v11
	v_cvt_pk_bf16_f32 v55, v2, v3
	v_lshlrev_b32_e32 v2, 16, v52
	v_and_b32_e32 v3, 0xffff0000, v52
	v_pk_add_f32 v[2:3], v[10:11], v[2:3] neg_lo:[0,1] neg_hi:[0,1]
	s_waitcnt vmcnt(32)
	v_cvt_pk_bf16_f32 v53, v8, v9
	v_cvt_pk_bf16_f32 v56, v2, v3
	v_lshlrev_b32_e32 v2, 16, v53
	v_and_b32_e32 v3, 0xffff0000, v53
	v_pk_add_f32 v[2:3], v[8:9], v[2:3] neg_lo:[0,1] neg_hi:[0,1]
	s_waitcnt vmcnt(30)
	v_cvt_pk_bf16_f32 v58, v64, v65
	v_cvt_pk_bf16_f32 v57, v2, v3
	v_lshlrev_b32_e32 v2, 16, v58
	v_and_b32_e32 v3, 0xffff0000, v58
	v_pk_add_f32 v[2:3], v[64:65], v[2:3] neg_lo:[0,1] neg_hi:[0,1]
	s_waitcnt vmcnt(28)
	v_cvt_pk_bf16_f32 v59, v66, v67
	v_cvt_pk_bf16_f32 v62, v2, v3
	v_lshlrev_b32_e32 v2, 16, v59
	v_and_b32_e32 v3, 0xffff0000, v59
	v_pk_add_f32 v[2:3], v[66:67], v[2:3] neg_lo:[0,1] neg_hi:[0,1]
	s_waitcnt vmcnt(26)
	v_cvt_pk_bf16_f32 v60, v68, v69
	v_cvt_pk_bf16_f32 v63, v2, v3
	v_lshlrev_b32_e32 v2, 16, v60
	v_and_b32_e32 v3, 0xffff0000, v60
	v_pk_add_f32 v[2:3], v[68:69], v[2:3] neg_lo:[0,1] neg_hi:[0,1]
	s_waitcnt vmcnt(24)
	v_cvt_pk_bf16_f32 v61, v16, v17
	v_cvt_pk_bf16_f32 v64, v2, v3
	v_lshlrev_b32_e32 v2, 16, v61
	v_and_b32_e32 v3, 0xffff0000, v61
	v_pk_add_f32 v[2:3], v[16:17], v[2:3] neg_lo:[0,1] neg_hi:[0,1]
	s_waitcnt vmcnt(22)
	v_cvt_pk_bf16_f32 v66, v72, v73
	v_cvt_pk_bf16_f32 v65, v2, v3
	v_lshlrev_b32_e32 v2, 16, v66
	v_and_b32_e32 v3, 0xffff0000, v66
	v_pk_add_f32 v[2:3], v[72:73], v[2:3] neg_lo:[0,1] neg_hi:[0,1]
	s_waitcnt vmcnt(20)
	v_cvt_pk_bf16_f32 v67, v74, v75
	v_cvt_pk_bf16_f32 v70, v2, v3
	v_lshlrev_b32_e32 v2, 16, v67
	v_and_b32_e32 v3, 0xffff0000, v67
	v_pk_add_f32 v[2:3], v[74:75], v[2:3] neg_lo:[0,1] neg_hi:[0,1]
	s_waitcnt vmcnt(18)
	v_cvt_pk_bf16_f32 v68, v76, v77
	v_cvt_pk_bf16_f32 v71, v2, v3
	v_lshlrev_b32_e32 v2, 16, v68
	v_and_b32_e32 v3, 0xffff0000, v68
	v_pk_add_f32 v[2:3], v[76:77], v[2:3] neg_lo:[0,1] neg_hi:[0,1]
	s_waitcnt vmcnt(16)
	v_cvt_pk_bf16_f32 v69, v78, v79
	v_cvt_pk_bf16_f32 v72, v2, v3
	v_lshlrev_b32_e32 v2, 16, v69
	v_and_b32_e32 v3, 0xffff0000, v69
	v_pk_add_f32 v[2:3], v[78:79], v[2:3] neg_lo:[0,1] neg_hi:[0,1]
	s_waitcnt vmcnt(14)
	v_cvt_pk_bf16_f32 v74, v80, v81
	s_add_u32 s58, s26, 0x4e000000
	v_cvt_pk_bf16_f32 v73, v2, v3
	v_lshlrev_b32_e32 v2, 16, v74
	v_and_b32_e32 v3, 0xffff0000, v74
	s_addc_u32 s59, s27, 0
	s_lshl_b32 s4, s82, 6
	v_pk_add_f32 v[2:3], v[80:81], v[2:3] neg_lo:[0,1] neg_hi:[0,1]
	s_waitcnt vmcnt(12)
	v_cvt_pk_bf16_f32 v75, v84, v85
	s_ashr_i32 s5, s4, 31
	v_cvt_pk_bf16_f32 v78, v2, v3
	v_lshlrev_b32_e32 v2, 16, v75
	v_and_b32_e32 v3, 0xffff0000, v75
	s_lshl_b64 s[4:5], s[4:5], 2
	v_pk_add_f32 v[2:3], v[84:85], v[2:3] neg_lo:[0,1] neg_hi:[0,1]
	s_waitcnt vmcnt(10)
	v_cvt_pk_bf16_f32 v76, v88, v89
	s_add_u32 s36, s26, s4
	v_cvt_pk_bf16_f32 v79, v2, v3
	v_lshlrev_b32_e32 v2, 16, v76
	v_and_b32_e32 v3, 0xffff0000, v76
	s_addc_u32 s37, s27, s5
	s_lshl_b32 s40, s82, 10
	v_pk_add_f32 v[2:3], v[88:89], v[2:3] neg_lo:[0,1] neg_hi:[0,1]
	s_waitcnt vmcnt(8)
	v_cvt_pk_bf16_f32 v77, v4, v5
	s_ashr_i32 s41, s40, 31
	v_cvt_pk_bf16_f32 v80, v2, v3
	v_lshlrev_b32_e32 v2, 16, v77
	v_and_b32_e32 v3, 0xffff0000, v77
	s_lshl_b64 s[4:5], s[40:41], 2
	v_pk_add_f32 v[2:3], v[4:5], v[2:3] neg_lo:[0,1] neg_hi:[0,1]
	v_ashrrev_i32_e32 v195, 31, v194
	s_add_u32 s46, s38, s4
	v_cvt_pk_bf16_f32 v81, v2, v3
	v_readlane_b32 s4, v254, 53
	v_lshlrev_b64 v[2:3], 3, v[194:195]
	s_addc_u32 s47, s39, s5
	v_add_u32_e32 v10, s4, v0
	v_lshl_add_u64 v[4:5], s[26:27], 0, v[2:3]
	s_mov_b64 s[4:5], 0x26000000
	v_lshl_add_u64 v[84:85], v[4:5], 0, s[4:5]
	v_and_b32_e32 v4, 15, v194
	v_mul_u32_u24_e32 v4, 0x810, v4
	v_lshlrev_b32_e32 v5, 4, v87
	v_readlane_b32 s4, v253, 17
	v_ashrrev_i32_e32 v193, 31, v192
	v_lshlrev_b64 v[6:7], 2, v[192:193]
	v_add3_u32 v11, v5, s4, v4
	s_movk_i32 s4, 0x100
	v_cmp_gt_i32_e64 s[48:49], s4, v192
	v_lshlrev_b32_e32 v5, 2, v192
	v_readlane_b32 s4, v254, 54
	v_lshl_add_u64 v[8:9], s[36:37], 0, v[6:7]
	v_lshl_add_u64 v[6:7], s[26:27], 0, v[6:7]
	v_add_u32_e32 v172, s4, v5
	v_readlane_b32 s4, v254, 55
	v_add_u32_e32 v4, s61, v87
	s_ashr_i32 s73, s72, 31
	v_add_u32_e32 v173, s4, v5
	s_mov_b64 s[4:5], 0x1000
	v_lshl_add_u64 v[90:91], v[8:9], 0, s[4:5]
	v_readlane_b32 s4, v254, 56
	v_lshlrev_b32_e32 v13, 7, v4
	v_lshl_add_u32 v12, v87, 9, v10
	v_add_u32_e32 v174, s4, v5
	v_readlane_b32 s4, v254, 57
	v_lshlrev_b32_e32 v168, 3, v194
	v_bitop3_b32 v86, v194, 31, v194 bitop3:0xc
	v_add_u32_e32 v175, s4, v5
	s_mov_b64 s[4:5], 0x1600000
	v_lshl_add_u64 v[92:93], v[6:7], 0, s[4:5]
	s_mov_b64 s[4:5], 0x1640000
	v_lshl_add_u64 v[94:95], v[6:7], 0, s[4:5]
	s_lshl_b64 s[4:5], s[72:73], 10
	v_ashrrev_i32_e32 v5, 31, v4
	v_lshl_add_u64 v[4:5], v[4:5], 4, s[4:5]
	v_lshl_add_u64 v[4:5], v[4:5], 0, v[0:1]
	v_lshl_add_u64 v[4:5], s[26:27], 0, v[4:5]
	s_mov_b64 s[4:5], 0x1680000
	v_lshl_add_u64 v[96:97], v[4:5], 0, s[4:5]
	v_readlane_b32 s4, v254, 9
	s_add_u32 s6, s26, s4
	v_readlane_b32 s4, v254, 10
	s_addc_u32 s14, s27, s4
	s_lshl_b64 s[4:5], s[72:73], 17
	s_add_u32 s4, s6, s4
	s_addc_u32 s5, s14, s5
	v_lshl_add_u64 v[98:99], s[4:5], 0, v[2:3]
	v_readlane_b32 s4, v254, 13
	s_add_u32 s6, s26, s4
	v_readlane_b32 s4, v254, 14
	s_addc_u32 s14, s27, s4
	s_lshl_b64 s[4:5], s[72:73], 16
	s_add_u32 s4, s6, s4
	v_lshlrev_b32_e32 v0, 2, v87
	s_addc_u32 s5, s14, s5
	v_add3_u32 v0, s29, v0, v82
	v_lshl_add_u64 v[100:101], v[194:195], 2, s[4:5]
	v_readlane_b32 s4, v253, 18
	v_cmp_gt_u32_e64 s[38:39], 4, v82
	v_cmp_eq_u32_e64 s[40:41], 0, v82
	v_cmp_eq_u32_e64 s[42:43], 1, v82
	v_cmp_eq_u32_e64 s[44:45], 2, v82
	v_lshl_add_u64 v[88:89], v[194:195], 4, s[46:47]
	v_add_u32_e32 v169, 0x200, v168
	v_add_u32_e32 v170, 0x400, v168
	v_add_u32_e32 v171, 0x600, v168
	v_cmp_gt_i32_e64 s[46:47], 32, v192
	v_ashrrev_i32_e32 v176, 2, v192
	v_lshl_add_u32 v177, v0, 2, 0
	v_add_u32_e32 v178, 0, v11
	v_add_u32_e32 v179, s4, v12
	v_add_u32_e32 v180, v10, v13
	s_mov_b32 s26, s72
	global_load_dwordx4 v[234:237], v[88:89], off
	global_load_dwordx4 v[238:241], v[88:89], off offset:1024
	global_load_dwordx4 v[242:245], v[88:89], off offset:2048
	global_load_dwordx4 v[246:249], v[88:89], off offset:3072
	s_branch .LBB0_479

.LBB0_479:
	s_and_saveexec_b64 s[36:37], s[46:47]
	ds_write_b32 v172, v1
	s_or_b64 exec, exec, s[36:37]
	s_ashr_i32 s27, s26, 31
	s_lshl_b64 s[4:5], s[26:27], 6
	s_add_u32 s4, s4, s61
	s_addc_u32 s5, s5, 0
	s_lshl_b64 s[4:5], s[4:5], 11
	v_lshl_add_u64 v[2:3], v[84:85], 0, s[4:5]
	s_waitcnt lgkmcnt(0)
	s_barrier
	s_cmp_lg_u32 s100, 0
	s_cbranch_scc1 .Lrr_skip
	global_load_dwordx2 v[102:103], v[2:3], off nt
	global_load_dwordx2 v[104:105], v[2:3], off offset:512 nt
	global_load_dwordx2 v[106:107], v[2:3], off offset:1024 nt
	global_load_dwordx2 v[108:109], v[2:3], off offset:1536 nt
	global_load_dwordx2 v[112:113], v[2:3], off offset:2048 nt
	global_load_dwordx2 v[118:119], v[2:3], off offset:2560 nt
	global_load_dwordx2 v[120:121], v[2:3], off offset:3072 nt
	global_load_dwordx2 v[122:123], v[2:3], off offset:3584 nt
.Lrr_skip:
	s_mov_b32 s100, 0
	s_mov_b32 s5, 0
	v_mov_b64_e32 v[110:111], v[100:101]
	v_mov_b64_e32 v[114:115], v[98:99]
	v_mov_b64_e32 v[116:117], v[96:97]
	s_branch .LBB0_483
